# P0 p to bf16 copy: added fast path, 4 chunks per iteration per wave, all loads 1KB contiguous and stores 512B contiguous, v_cvt_pk_bf16_f32 (RNE, same as bit trick)
# speedup vs baseline: 1.0135x; 1.0007x over previous
.LBB0_242:
	s_or_b64 exec, exec, s[18:19]
	v_readfirstlane_b32 s4, v6
	v_lshlrev_b32_e32 v96, 4, v55
	v_lshlrev_b32_e32 v97, 3, v55
	s_mul_i32 s5, s10, 3
	s_lshl_b32 s6, s10, 5
	s_lshl_b32 s7, s10, 4
	s_lshl_b32 s11, s10, 2
.Lpcv_loop:
	s_add_u32 s8, s4, s5
	s_cmp_lt_u32 s8, 0x400000
	s_cbranch_scc0 .Lpcv_done
	s_lshl_b32 s9, s4, 5
	s_add_u32 s32, s14, s9
	s_addc_u32 s33, s15, 0
	s_lshl_b32 s9, s4, 4
	s_add_u32 s34, s52, 0x1ac00000
	s_addc_u32 s35, s53, 0
	s_add_u32 s34, s34, s9
	s_addc_u32 s35, s35, 0
	s_mov_b64 s[36:37], s[32:33]
	global_load_dwordx4 v[64:67], v96, s[36:37]
	global_load_dwordx4 v[68:71], v96, s[36:37] offset:1024
	s_add_u32 s32, s32, s6
	s_addc_u32 s33, s33, 0
	s_mov_b64 s[38:39], s[32:33]
	global_load_dwordx4 v[72:75], v96, s[38:39]
	global_load_dwordx4 v[76:79], v96, s[38:39] offset:1024
	s_add_u32 s32, s32, s6
	s_addc_u32 s33, s33, 0
	s_mov_b64 s[36:37], s[32:33]
	global_load_dwordx4 v[80:83], v96, s[36:37]
	global_load_dwordx4 v[84:87], v96, s[36:37] offset:1024
	s_add_u32 s32, s32, s6
	s_addc_u32 s33, s33, 0
	s_mov_b64 s[38:39], s[32:33]
	global_load_dwordx4 v[88:91], v96, s[38:39]
	global_load_dwordx4 v[92:95], v96, s[38:39] offset:1024
	s_add_u32 s32, s32, s6
	s_addc_u32 s33, s33, 0
	s_waitcnt vmcnt(6)
	s_mov_b64 s[36:37], s[34:35]
	v_cvt_pk_bf16_f32 v130, v64, v65
	v_cvt_pk_bf16_f32 v131, v66, v67
	v_cvt_pk_bf16_f32 v132, v68, v69
	v_cvt_pk_bf16_f32 v133, v70, v71
	global_store_dwordx2 v97, v[130:131], s[36:37]
	global_store_dwordx2 v97, v[132:133], s[36:37] offset:512
	s_add_u32 s34, s34, s7
	s_addc_u32 s35, s35, 0
	s_waitcnt vmcnt(6)
	s_mov_b64 s[38:39], s[34:35]
	v_cvt_pk_bf16_f32 v134, v72, v73
	v_cvt_pk_bf16_f32 v135, v74, v75
	v_cvt_pk_bf16_f32 v136, v76, v77
	v_cvt_pk_bf16_f32 v137, v78, v79
	global_store_dwordx2 v97, v[134:135], s[38:39]
	global_store_dwordx2 v97, v[136:137], s[38:39] offset:512
	s_add_u32 s34, s34, s7
	s_addc_u32 s35, s35, 0
	s_waitcnt vmcnt(6)
	s_mov_b64 s[36:37], s[34:35]
	v_cvt_pk_bf16_f32 v138, v80, v81
	v_cvt_pk_bf16_f32 v139, v82, v83
	v_cvt_pk_bf16_f32 v140, v84, v85
	v_cvt_pk_bf16_f32 v141, v86, v87
	global_store_dwordx2 v97, v[138:139], s[36:37]
	global_store_dwordx2 v97, v[140:141], s[36:37] offset:512
	s_add_u32 s34, s34, s7
	s_addc_u32 s35, s35, 0
	s_waitcnt vmcnt(6)
	s_mov_b64 s[38:39], s[34:35]
	v_cvt_pk_bf16_f32 v142, v88, v89
	v_cvt_pk_bf16_f32 v143, v90, v91
	v_cvt_pk_bf16_f32 v144, v92, v93
	v_cvt_pk_bf16_f32 v145, v94, v95
	global_store_dwordx2 v97, v[142:143], s[38:39]
	global_store_dwordx2 v97, v[144:145], s[38:39] offset:512
	s_add_u32 s34, s34, s7
	s_addc_u32 s35, s35, 0
	s_add_u32 s4, s4, s11
	v_add_u32_e32 v6, s11, v6
	s_branch .Lpcv_loop
.Lpcv_done:
	s_mov_b32 s1, 0x400000
	v_cmp_gt_u32_e32 vcc, s1, v6
	s_and_saveexec_b64 s[6:7], vcc
	s_cbranch_execz .LBB0_245
	v_mov_b32_e32 v7, 0
	v_lshlrev_b64 v[2:3], 5, v[6:7]
	s_ashr_i32 s11, s10, 31
	v_lshl_add_u64 v[2:3], s[14:15], 0, v[2:3]
	v_lshl_add_u64 v[4:5], v[6:7], 4, v[34:35]
	s_mov_b64 s[4:5], 0x1ac00000
	v_lshl_add_u64 v[2:3], v[2:3], 0, 16
	s_lshl_b64 s[8:9], s[10:11], 5
	v_lshl_add_u64 v[4:5], v[4:5], 0, s[4:5]
	s_lshl_b64 s[14:15], s[10:11], 4
	s_mov_b64 s[18:19], 0
	s_movk_i32 s1, 0x7fff
	s_mov_b32 s4, 0xffff0000
	s_mov_b64 s[20:21], 0x3fffff
